# v22 + FOX tile loop steady-state fast paths for DMA issue and counted waits
# speedup vs baseline: 1.0071x; 1.0063x over previous
; #define ISSUE_K(t, sl) do { glds16(Kg + (long)(t) * (KSLOT / 2), (unsigned)__builtin_amdgcn_readfirstlane(kdst + (sl) * KSLOT)); \
;         if (k2) glds16(Kg + (long)(t) * (KSLOT / 2) + 4096, (unsigned)__builtin_amdgcn_readfirstlane(kdst + (sl) * KSLOT + 8192)); } while (0)
; #define ISSUE_V(t, sl) glds16(Vg + (long)(t) * 4096, (unsigned)__builtin_amdgcn_readfirstlane(vdst + (sl) * VSLOT))
; template <bool FOX>
; __device__ __forceinline__ void attn_unit(const Args& A, int b, int h, int qb, LAS char* shm, LAS float* dg) {
;     ...
;         if (t == 1 && 4 < nti) ISSUE_K(t0 + 4, 0);
;         if (t + 4 < nti) ISSUE_K(t0 + t + 4, t % NS);
;         if (t + 2 < nti) ISSUE_V(t0 + t + 2, (t + 2) % NS);
.LBB0_950:
	s_cmp_eq_u32 s52, 0
	s_cbranch_scc1 .Lfox_slow_top
	s_add_i32 s26, s53, 4
	s_cmp_lt_i32 s26, s6
	s_cbranch_scc0 .Lfox_slow_top
	s_add_i32 s26, s14, s52
	s_add_i32 s26, s26, 5
	s_ashr_i32 s27, s26, 31
	s_lshl_b64 s[26:27], s[26:27], 13
	v_lshl_add_u64 v[158:159], v[132:133], 0, s[26:27]
	s_add_i32 s26, s38, 0xffffa000
	s_and_b32 s26, s26, 0x6000
	s_add_i32 m0, s26, s4
	s_add_i32 s26, s14, s52
	global_load_lds_dwordx4 v[158:159], off
	s_add_i32 s26, s26, 3
	s_ashr_i32 s27, s26, 31
	s_lshl_b64 s[26:27], s[26:27], 13
	v_lshl_add_u64 v[158:159], v[186:187], 0, s[26:27]
	s_add_i32 s26, s38, 0xffffe000
	s_and_b32 s26, s26, 0x6000
	s_add_i32 m0, s26, s5
	s_mov_b64 s[40:41], -1
	global_load_lds_dwordx4 v[158:159], off
	s_mov_b64 s[42:43], -1
	s_branch .LBB0_956

; #define WAITV(n) do { switch (n) { WV_(0) WV_(1) WV_(2) WV_(3) WV_(4) WV_(5) default: asm volatile("s_waitcnt vmcnt(6)" ::: "memory"); break; } } while (0)
; template <bool FOX>
; __device__ __forceinline__ void attn_unit(const Args& A, int b, int h, int qb, LAS char* shm, LAS float* dg) {
;     ...
;         WAITV(((t + 3 < nti ? nK : 0) + (t + 1 < nti ? 1 : 0)) + ((t + 4 < nti ? nK : 0) + (t + 2 < nti ? 1 : 0)));
.LBB0_964:
	s_add_i32 s26, s53, 1
	s_and_b64 vcc, exec, s[40:41]
	s_cbranch_vccz .Lfox_slow_tail
	s_waitcnt vmcnt(4)
	s_branch .LBB0_978
.Lfox_slow_tail:
	s_add_i32 s27, s53, 3
	s_cmp_lt_i32 s27, s6
	s_cselect_b64 s[44:45], -1, 0
	s_cmp_lt_i32 s26, s6
	s_cselect_b64 s[46:47], -1, 0
	v_cndmask_b32_e64 v130, 0, 1, s[46:47]
	v_cndmask_b32_e64 v159, 0, 1, s[42:43]
	v_cndmask_b32_e64 v158, 0, 1, s[40:41]
	v_readfirstlane_b32 s27, v159
	v_readfirstlane_b32 s40, v130
	s_cmp_lg_u64 s[44:45], 0
	s_addc_u32 s27, s27, s40
	v_readfirstlane_b32 s40, v158
	s_add_i32 s27, s27, s40
	s_cmp_lt_i32 s27, 3
	s_mov_b64 s[40:41], -1
	s_cbranch_scc1 .LBB0_970
	s_cmp_gt_i32 s27, 3
	s_cbranch_scc0 .LBB0_967
	s_waitcnt vmcnt(4)
	s_mov_b64 s[40:41], 0
